# P8 router tail: the last three slot atomics of a token issued together (one wait for all four) instead of atomic-wait-store x4
# baseline (speedup 1.0000x reference)
.LBB0_1277:
	s_waitcnt lgkmcnt(0)
	v_cmp_gt_u32_e32 vcc, 16, v33
	s_and_b64 s[8:9], vcc, s[8:9]
	s_and_b64 s[8:9], s[4:5], s[8:9]
	s_and_saveexec_b64 s[4:5], s[8:9]
	s_cbranch_execz .LBB0_1279
	v_mov_b32_e32 v5, 0
	global_load_dwordx4 v[6:9], v5, s[10:11]
	global_load_dwordx4 v[10:13], v5, s[10:11] offset:16
	global_load_dwordx4 v[16:19], v5, s[10:11] offset:32
	global_load_dwordx4 v[20:23], v5, s[10:11] offset:48
	global_load_dwordx4 v[24:27], v5, s[10:11] offset:64
	global_load_dwordx4 v[28:31], v5, s[10:11] offset:80
	global_load_dwordx4 v[34:37], v5, s[10:11] offset:96
	global_load_dwordx4 v[38:41], v5, s[10:11] offset:112
	v_or_b32_e32 v14, s2, v33
	s_movk_i32 s2, 0x84
	v_mov_b32_e32 v1, s12
	v_mad_u32_u24 v1, v33, s2, v1
	ds_read2_b32 v[2:3], v1 offset1:1
	ds_read2_b32 v[32:33], v1 offset0:2 offset1:3
	ds_read2_b32 v[42:43], v1 offset0:4 offset1:5
	ds_read2_b32 v[44:45], v1 offset0:6 offset1:7
	ds_read2_b32 v[46:47], v1 offset0:8 offset1:9
	ds_read2_b32 v[48:49], v1 offset0:10 offset1:11
	ds_read2_b32 v[50:51], v1 offset0:12 offset1:13
	ds_read2_b32 v[52:53], v1 offset0:14 offset1:15
	ds_read2_b32 v[54:55], v1 offset0:16 offset1:17
	ds_read2_b32 v[56:57], v1 offset0:18 offset1:19
	ds_read2_b32 v[58:59], v1 offset0:20 offset1:21
	ds_read2_b32 v[60:61], v1 offset0:22 offset1:23
	ds_read2_b32 v[62:63], v1 offset0:24 offset1:25
	ds_read2_b32 v[64:65], v1 offset0:26 offset1:27
	ds_read2_b32 v[66:67], v1 offset0:28 offset1:29
	ds_read2_b32 v[68:69], v1 offset0:30 offset1:31
	s_add_u32 s10, s6, 0x4600
	s_addc_u32 s11, s7, 0
	s_add_u32 s8, s6, 0x5f30000
	s_addc_u32 s9, s7, 0
	s_waitcnt vmcnt(7) lgkmcnt(14)
	v_add_f32_e32 v1, v2, v6
	v_add_f32_e32 v4, v3, v7
	v_max_f32_e32 v2, 0xff800000, v1
	v_cmp_gt_f32_e32 vcc, v4, v2
	v_add_f32_e32 v6, v32, v8
	v_add_f32_e32 v7, v33, v9
	v_cndmask_b32_e32 v2, v2, v4, vcc
	v_cndmask_b32_e64 v3, 0, 1, vcc
	v_cmp_gt_f32_e32 vcc, v6, v2
	s_waitcnt vmcnt(6) lgkmcnt(13)
	v_add_f32_e32 v8, v42, v10
	v_add_f32_e32 v9, v43, v11
	v_cndmask_b32_e32 v2, v2, v6, vcc
	v_cndmask_b32_e64 v3, v3, 2, vcc
	v_cmp_gt_f32_e32 vcc, v7, v2
	s_waitcnt lgkmcnt(12)
	v_add_f32_e32 v10, v44, v12
	v_add_f32_e32 v11, v45, v13
	v_cndmask_b32_e32 v2, v2, v7, vcc
	v_cndmask_b32_e64 v3, v3, 3, vcc
	v_cmp_gt_f32_e32 vcc, v8, v2
	s_waitcnt vmcnt(5) lgkmcnt(11)
	v_add_f32_e32 v12, v46, v16
	v_add_f32_e32 v13, v47, v17
	v_cndmask_b32_e32 v2, v2, v8, vcc
	v_cndmask_b32_e64 v3, v3, 4, vcc
	v_cmp_gt_f32_e32 vcc, v9, v2
	s_waitcnt lgkmcnt(10)
	v_add_f32_e32 v15, v48, v18
	v_add_f32_e32 v16, v49, v19
	v_cndmask_b32_e32 v2, v2, v9, vcc
	v_cndmask_b32_e64 v3, v3, 5, vcc
	v_cmp_gt_f32_e32 vcc, v10, v2
	s_waitcnt vmcnt(4) lgkmcnt(9)
	v_add_f32_e32 v17, v50, v20
	v_add_f32_e32 v18, v51, v21
	v_cndmask_b32_e32 v2, v2, v10, vcc
	v_cndmask_b32_e64 v3, v3, 6, vcc
	v_cmp_gt_f32_e32 vcc, v11, v2
	s_waitcnt lgkmcnt(8)
	v_add_f32_e32 v19, v52, v22
	v_add_f32_e32 v20, v53, v23
	v_cndmask_b32_e32 v2, v2, v11, vcc
	v_cndmask_b32_e64 v3, v3, 7, vcc
	v_cmp_gt_f32_e32 vcc, v12, v2
	s_waitcnt vmcnt(3) lgkmcnt(7)
	v_add_f32_e32 v21, v54, v24
	v_add_f32_e32 v22, v55, v25
	v_cndmask_b32_e32 v2, v2, v12, vcc
	v_cndmask_b32_e64 v3, v3, 8, vcc
	v_cmp_gt_f32_e32 vcc, v13, v2
	s_waitcnt lgkmcnt(6)
	v_add_f32_e32 v23, v56, v26
	v_add_f32_e32 v24, v57, v27
	v_cndmask_b32_e32 v2, v2, v13, vcc
	v_cndmask_b32_e64 v3, v3, 9, vcc
	v_cmp_gt_f32_e32 vcc, v15, v2
	s_waitcnt vmcnt(2) lgkmcnt(5)
	v_add_f32_e32 v25, v58, v28
	v_add_f32_e32 v26, v59, v29
	v_cndmask_b32_e32 v2, v2, v15, vcc
	v_cndmask_b32_e64 v3, v3, 10, vcc
	v_cmp_gt_f32_e32 vcc, v16, v2
	s_waitcnt lgkmcnt(4)
	v_add_f32_e32 v27, v60, v30
	v_add_f32_e32 v28, v61, v31
	v_cndmask_b32_e32 v2, v2, v16, vcc
	v_cndmask_b32_e64 v3, v3, 11, vcc
	v_cmp_gt_f32_e32 vcc, v17, v2
	s_waitcnt vmcnt(1) lgkmcnt(3)
	v_add_f32_e32 v29, v62, v34
	v_add_f32_e32 v30, v63, v35
	v_cndmask_b32_e32 v2, v2, v17, vcc
	v_cndmask_b32_e64 v3, v3, 12, vcc
	v_cmp_gt_f32_e32 vcc, v18, v2
	s_waitcnt lgkmcnt(2)
	v_add_f32_e32 v31, v64, v36
	v_add_f32_e32 v32, v65, v37
	v_cndmask_b32_e32 v2, v2, v18, vcc
	v_cndmask_b32_e64 v3, v3, 13, vcc
	v_cmp_gt_f32_e32 vcc, v19, v2
	s_waitcnt vmcnt(0) lgkmcnt(1)
	v_add_f32_e32 v33, v66, v38
	v_add_f32_e32 v34, v67, v39
	v_cndmask_b32_e32 v2, v2, v19, vcc
	v_cndmask_b32_e64 v3, v3, 14, vcc
	v_cmp_gt_f32_e32 vcc, v20, v2
	s_waitcnt lgkmcnt(0)
	v_add_f32_e32 v35, v68, v40
	v_add_f32_e32 v36, v69, v41
	v_cndmask_b32_e32 v2, v2, v20, vcc
	v_cndmask_b32_e64 v3, v3, 15, vcc
	v_cmp_gt_f32_e32 vcc, v21, v2
	s_nop 1
	v_cndmask_b32_e32 v2, v2, v21, vcc
	v_cndmask_b32_e64 v3, v3, 16, vcc
	v_cmp_gt_f32_e32 vcc, v22, v2
	s_nop 1
	v_cndmask_b32_e32 v2, v2, v22, vcc
	v_cndmask_b32_e64 v3, v3, 17, vcc
	v_cmp_gt_f32_e32 vcc, v23, v2
	s_nop 1
	v_cndmask_b32_e32 v2, v2, v23, vcc
	v_cndmask_b32_e64 v3, v3, 18, vcc
	v_cmp_gt_f32_e32 vcc, v24, v2
	s_nop 1
	v_cndmask_b32_e32 v2, v2, v24, vcc
	v_cndmask_b32_e64 v3, v3, 19, vcc
	v_cmp_gt_f32_e32 vcc, v25, v2
	s_nop 1
	v_cndmask_b32_e32 v2, v2, v25, vcc
	v_cndmask_b32_e64 v3, v3, 20, vcc
	v_cmp_gt_f32_e32 vcc, v26, v2
	s_nop 1
	v_cndmask_b32_e32 v2, v2, v26, vcc
	v_cndmask_b32_e64 v3, v3, 21, vcc
	v_cmp_gt_f32_e32 vcc, v27, v2
	s_nop 1
	v_cndmask_b32_e32 v2, v2, v27, vcc
	v_cndmask_b32_e64 v3, v3, 22, vcc
	v_cmp_gt_f32_e32 vcc, v28, v2
	s_nop 1
	v_cndmask_b32_e32 v2, v2, v28, vcc
	v_cndmask_b32_e64 v3, v3, 23, vcc
	v_cmp_gt_f32_e32 vcc, v29, v2
	s_nop 1
	v_cndmask_b32_e32 v2, v2, v29, vcc
	v_cndmask_b32_e64 v3, v3, 24, vcc
	v_cmp_gt_f32_e32 vcc, v30, v2
	s_nop 1
	v_cndmask_b32_e32 v2, v2, v30, vcc
	v_cndmask_b32_e64 v3, v3, 25, vcc
	v_cmp_gt_f32_e32 vcc, v31, v2
	s_nop 1
	v_cndmask_b32_e32 v2, v2, v31, vcc
	v_cndmask_b32_e64 v3, v3, 26, vcc
	v_cmp_gt_f32_e32 vcc, v32, v2
	s_nop 1
	v_cndmask_b32_e32 v2, v2, v32, vcc
	v_cndmask_b32_e64 v3, v3, 27, vcc
	v_cmp_gt_f32_e32 vcc, v33, v2
	s_nop 1
	v_cndmask_b32_e32 v2, v2, v33, vcc
	v_cndmask_b32_e64 v3, v3, 28, vcc
	v_cmp_gt_f32_e32 vcc, v34, v2
	s_nop 1
	v_cndmask_b32_e32 v2, v2, v34, vcc
	v_cndmask_b32_e64 v3, v3, 29, vcc
	v_cmp_gt_f32_e32 vcc, v35, v2
	s_nop 1
	v_cndmask_b32_e32 v37, v2, v35, vcc
	v_cndmask_b32_e64 v3, v3, 30, vcc
	v_cmp_gt_f32_e32 vcc, v36, v37
	s_nop 1
	v_cndmask_b32_e64 v2, v3, 31, vcc
	v_cndmask_b32_e32 v3, v37, v36, vcc
	v_mov_b32_e32 v37, 0xff800000
	v_cmp_ne_u32_e32 vcc, 0, v2
	s_nop 1
	v_cndmask_b32_e32 v38, v37, v1, vcc
	v_cmp_ne_u32_e32 vcc, 1, v2
	v_mov_b32_e32 v1, 1
	s_nop 0
	v_cndmask_b32_e32 v4, v37, v4, vcc
	v_cmp_ne_u32_e32 vcc, 2, v2
	s_nop 1
	v_cndmask_b32_e32 v39, v37, v6, vcc
	v_cmp_ne_u32_e32 vcc, 3, v2
	v_max_f32_e32 v6, 0xff800000, v38
	s_nop 0
	v_cndmask_b32_e32 v7, v37, v7, vcc
	v_cmp_ne_u32_e32 vcc, 4, v2
	s_nop 1
	v_cndmask_b32_e32 v8, v37, v8, vcc
	v_cmp_ne_u32_e32 vcc, 5, v2
	s_nop 1
	v_cndmask_b32_e32 v9, v37, v9, vcc
	v_cmp_ne_u32_e32 vcc, 6, v2
	s_nop 1
	v_cndmask_b32_e32 v10, v37, v10, vcc
	v_cmp_ne_u32_e32 vcc, 7, v2
	s_nop 1
	v_cndmask_b32_e32 v11, v37, v11, vcc
	v_cmp_ne_u32_e32 vcc, 8, v2
	s_nop 1
	v_cndmask_b32_e32 v12, v37, v12, vcc
	v_cmp_ne_u32_e32 vcc, 9, v2
	s_nop 1
	v_cndmask_b32_e32 v13, v37, v13, vcc
	v_cmp_ne_u32_e32 vcc, 10, v2
	s_nop 1
	v_cndmask_b32_e32 v15, v37, v15, vcc
	v_cmp_ne_u32_e32 vcc, 11, v2
	s_nop 1
	v_cndmask_b32_e32 v16, v37, v16, vcc
	v_cmp_ne_u32_e32 vcc, 12, v2
	s_nop 1
	v_cndmask_b32_e32 v17, v37, v17, vcc
	v_cmp_ne_u32_e32 vcc, 13, v2
	s_nop 1
	v_cndmask_b32_e32 v18, v37, v18, vcc
	v_cmp_ne_u32_e32 vcc, 14, v2
	s_nop 1
	v_cndmask_b32_e32 v19, v37, v19, vcc
	v_cmp_ne_u32_e32 vcc, 15, v2
	s_nop 1
	v_cndmask_b32_e32 v20, v37, v20, vcc
	v_cmp_ne_u32_e32 vcc, 16, v2
	s_nop 1
	v_cndmask_b32_e32 v21, v37, v21, vcc
	v_cmp_ne_u32_e32 vcc, 17, v2
	s_nop 1
	v_cndmask_b32_e32 v22, v37, v22, vcc
	v_cmp_ne_u32_e32 vcc, 18, v2
	s_nop 1
	v_cndmask_b32_e32 v23, v37, v23, vcc
	v_cmp_ne_u32_e32 vcc, 19, v2
	s_nop 1
	v_cndmask_b32_e32 v24, v37, v24, vcc
	v_cmp_ne_u32_e32 vcc, 20, v2
	s_nop 1
	v_cndmask_b32_e32 v25, v37, v25, vcc
	v_cmp_ne_u32_e32 vcc, 21, v2
	s_nop 1
	v_cndmask_b32_e32 v26, v37, v26, vcc
	v_cmp_ne_u32_e32 vcc, 22, v2
	s_nop 1
	v_cndmask_b32_e32 v27, v37, v27, vcc
	v_cmp_ne_u32_e32 vcc, 23, v2
	s_nop 1
	v_cndmask_b32_e32 v28, v37, v28, vcc
	v_cmp_ne_u32_e32 vcc, 24, v2
	s_nop 1
	v_cndmask_b32_e32 v29, v37, v29, vcc
	v_cmp_ne_u32_e32 vcc, 25, v2
	s_nop 1
	v_cndmask_b32_e32 v30, v37, v30, vcc
	v_cmp_ne_u32_e32 vcc, 26, v2
	s_nop 1
	v_cndmask_b32_e32 v31, v37, v31, vcc
	v_cmp_ne_u32_e32 vcc, 27, v2
	s_nop 1
	v_cndmask_b32_e32 v32, v37, v32, vcc
	v_cmp_ne_u32_e32 vcc, 28, v2
	s_nop 1
	v_cndmask_b32_e32 v33, v37, v33, vcc
	v_cmp_ne_u32_e32 vcc, 29, v2
	s_nop 1
	v_cndmask_b32_e32 v34, v37, v34, vcc
	v_cmp_ne_u32_e32 vcc, 30, v2
	s_nop 1
	v_cndmask_b32_e32 v35, v37, v35, vcc
	v_cmp_ne_u32_e32 vcc, 31, v2
	s_nop 1
	v_cndmask_b32_e32 v36, v37, v36, vcc
	v_cmp_gt_f32_e32 vcc, v4, v6
	s_nop 1
	v_cndmask_b32_e32 v6, v6, v4, vcc
	v_cndmask_b32_e64 v40, 0, 1, vcc
	v_cmp_gt_f32_e32 vcc, v39, v6
	s_nop 1
	v_cndmask_b32_e32 v6, v6, v39, vcc
	v_cndmask_b32_e64 v40, v40, 2, vcc
	v_cmp_gt_f32_e32 vcc, v7, v6
	s_nop 1
	v_cndmask_b32_e32 v6, v6, v7, vcc
	v_cndmask_b32_e64 v40, v40, 3, vcc
	v_cmp_gt_f32_e32 vcc, v8, v6
	s_nop 1
	v_cndmask_b32_e32 v6, v6, v8, vcc
	v_cndmask_b32_e64 v40, v40, 4, vcc
	v_cmp_gt_f32_e32 vcc, v9, v6
	s_nop 1
	v_cndmask_b32_e32 v6, v6, v9, vcc
	v_cndmask_b32_e64 v40, v40, 5, vcc
	v_cmp_gt_f32_e32 vcc, v10, v6
	s_nop 1
	v_cndmask_b32_e32 v6, v6, v10, vcc
	v_cndmask_b32_e64 v40, v40, 6, vcc
	v_cmp_gt_f32_e32 vcc, v11, v6
	s_nop 1
	v_cndmask_b32_e32 v6, v6, v11, vcc
	v_cndmask_b32_e64 v40, v40, 7, vcc
	v_cmp_gt_f32_e32 vcc, v12, v6
	s_nop 1
	v_cndmask_b32_e32 v6, v6, v12, vcc
	v_cndmask_b32_e64 v40, v40, 8, vcc
	v_cmp_gt_f32_e32 vcc, v13, v6
	s_nop 1
	v_cndmask_b32_e32 v6, v6, v13, vcc
	v_cndmask_b32_e64 v40, v40, 9, vcc
	v_cmp_gt_f32_e32 vcc, v15, v6
	s_nop 1
	v_cndmask_b32_e32 v6, v6, v15, vcc
	v_cndmask_b32_e64 v40, v40, 10, vcc
	v_cmp_gt_f32_e32 vcc, v16, v6
	s_nop 1
	v_cndmask_b32_e32 v6, v6, v16, vcc
	v_cndmask_b32_e64 v40, v40, 11, vcc
	v_cmp_gt_f32_e32 vcc, v17, v6
	s_nop 1
	v_cndmask_b32_e32 v6, v6, v17, vcc
	v_cndmask_b32_e64 v40, v40, 12, vcc
	v_cmp_gt_f32_e32 vcc, v18, v6
	s_nop 1
	v_cndmask_b32_e32 v6, v6, v18, vcc
	v_cndmask_b32_e64 v40, v40, 13, vcc
	v_cmp_gt_f32_e32 vcc, v19, v6
	s_nop 1
	v_cndmask_b32_e32 v6, v6, v19, vcc
	v_cndmask_b32_e64 v40, v40, 14, vcc
	v_cmp_gt_f32_e32 vcc, v20, v6
	s_nop 1
	v_cndmask_b32_e32 v6, v6, v20, vcc
	v_cndmask_b32_e64 v40, v40, 15, vcc
	v_cmp_gt_f32_e32 vcc, v21, v6
	s_nop 1
	v_cndmask_b32_e32 v6, v6, v21, vcc
	v_cndmask_b32_e64 v40, v40, 16, vcc
	v_cmp_gt_f32_e32 vcc, v22, v6
	s_nop 1
	v_cndmask_b32_e32 v6, v6, v22, vcc
	v_cndmask_b32_e64 v40, v40, 17, vcc
	v_cmp_gt_f32_e32 vcc, v23, v6
	s_nop 1
	v_cndmask_b32_e32 v6, v6, v23, vcc
	v_cndmask_b32_e64 v40, v40, 18, vcc
	v_cmp_gt_f32_e32 vcc, v24, v6
	s_nop 1
	v_cndmask_b32_e32 v6, v6, v24, vcc
	v_cndmask_b32_e64 v40, v40, 19, vcc
	v_cmp_gt_f32_e32 vcc, v25, v6
	s_nop 1
	v_cndmask_b32_e32 v6, v6, v25, vcc
	v_cndmask_b32_e64 v40, v40, 20, vcc
	v_cmp_gt_f32_e32 vcc, v26, v6
	s_nop 1
	v_cndmask_b32_e32 v6, v6, v26, vcc
	v_cndmask_b32_e64 v40, v40, 21, vcc
	v_cmp_gt_f32_e32 vcc, v27, v6
	s_nop 1
	v_cndmask_b32_e32 v6, v6, v27, vcc
	v_cndmask_b32_e64 v40, v40, 22, vcc
	v_cmp_gt_f32_e32 vcc, v28, v6
	s_nop 1
	v_cndmask_b32_e32 v6, v6, v28, vcc
	v_cndmask_b32_e64 v40, v40, 23, vcc
	v_cmp_gt_f32_e32 vcc, v29, v6
	s_nop 1
	v_cndmask_b32_e32 v6, v6, v29, vcc
	v_cndmask_b32_e64 v40, v40, 24, vcc
	v_cmp_gt_f32_e32 vcc, v30, v6
	s_nop 1
	v_cndmask_b32_e32 v6, v6, v30, vcc
	v_cndmask_b32_e64 v40, v40, 25, vcc
	v_cmp_gt_f32_e32 vcc, v31, v6
	s_nop 1
	v_cndmask_b32_e32 v6, v6, v31, vcc
	v_cndmask_b32_e64 v40, v40, 26, vcc
	v_cmp_gt_f32_e32 vcc, v32, v6
	s_nop 1
	v_cndmask_b32_e32 v6, v6, v32, vcc
	v_cndmask_b32_e64 v40, v40, 27, vcc
	v_cmp_gt_f32_e32 vcc, v33, v6
	s_nop 1
	v_cndmask_b32_e32 v6, v6, v33, vcc
	v_cndmask_b32_e64 v40, v40, 28, vcc
	v_cmp_gt_f32_e32 vcc, v34, v6
	s_nop 1
	v_cndmask_b32_e32 v6, v6, v34, vcc
	v_cndmask_b32_e64 v40, v40, 29, vcc
	v_cmp_gt_f32_e32 vcc, v35, v6
	s_nop 1
	v_cndmask_b32_e32 v41, v6, v35, vcc
	v_cndmask_b32_e64 v40, v40, 30, vcc
	v_cmp_gt_f32_e32 vcc, v36, v41
	s_nop 1
	v_cndmask_b32_e64 v6, v40, 31, vcc
	v_cndmask_b32_e32 v40, v41, v36, vcc
	v_cmp_ne_u32_e32 vcc, 0, v6
	s_nop 1
	v_cndmask_b32_e32 v38, v37, v38, vcc
	v_cmp_ne_u32_e32 vcc, 1, v6
	s_nop 1
	v_cndmask_b32_e32 v4, v37, v4, vcc
	v_cmp_ne_u32_e32 vcc, 2, v6
	s_nop 1
	v_cndmask_b32_e32 v39, v37, v39, vcc
	v_cmp_ne_u32_e32 vcc, 3, v6
	s_nop 1
	v_cndmask_b32_e32 v7, v37, v7, vcc
	v_cmp_ne_u32_e32 vcc, 4, v6
	s_nop 1
	v_cndmask_b32_e32 v8, v37, v8, vcc
	v_cmp_ne_u32_e32 vcc, 5, v6
	s_nop 1
	v_cndmask_b32_e32 v9, v37, v9, vcc
	v_cmp_ne_u32_e32 vcc, 6, v6
	s_nop 1
	v_cndmask_b32_e32 v41, v37, v10, vcc
	v_cmp_ne_u32_e32 vcc, 7, v6
	v_max_f32_e32 v10, 0xff800000, v38
	s_nop 0
	v_cndmask_b32_e32 v11, v37, v11, vcc
	v_cmp_ne_u32_e32 vcc, 8, v6
	s_nop 1
	v_cndmask_b32_e32 v12, v37, v12, vcc
	v_cmp_ne_u32_e32 vcc, 9, v6
	s_nop 1
	v_cndmask_b32_e32 v13, v37, v13, vcc
	v_cmp_ne_u32_e32 vcc, 10, v6
	s_nop 1
	v_cndmask_b32_e32 v15, v37, v15, vcc
	v_cmp_ne_u32_e32 vcc, 11, v6
	s_nop 1
	v_cndmask_b32_e32 v16, v37, v16, vcc
	v_cmp_ne_u32_e32 vcc, 12, v6
	s_nop 1
	v_cndmask_b32_e32 v17, v37, v17, vcc
	v_cmp_ne_u32_e32 vcc, 13, v6
	s_nop 1
	v_cndmask_b32_e32 v18, v37, v18, vcc
	v_cmp_ne_u32_e32 vcc, 14, v6
	s_nop 1
	v_cndmask_b32_e32 v19, v37, v19, vcc
	v_cmp_ne_u32_e32 vcc, 15, v6
	s_nop 1
	v_cndmask_b32_e32 v20, v37, v20, vcc
	v_cmp_ne_u32_e32 vcc, 16, v6
	s_nop 1
	v_cndmask_b32_e32 v21, v37, v21, vcc
	v_cmp_ne_u32_e32 vcc, 17, v6
	s_nop 1
	v_cndmask_b32_e32 v22, v37, v22, vcc
	v_cmp_ne_u32_e32 vcc, 18, v6
	s_nop 1
	v_cndmask_b32_e32 v23, v37, v23, vcc
	v_cmp_ne_u32_e32 vcc, 19, v6
	s_nop 1
	v_cndmask_b32_e32 v24, v37, v24, vcc
	v_cmp_ne_u32_e32 vcc, 20, v6
	s_nop 1
	v_cndmask_b32_e32 v25, v37, v25, vcc
	v_cmp_ne_u32_e32 vcc, 21, v6
	s_nop 1
	v_cndmask_b32_e32 v26, v37, v26, vcc
	v_cmp_ne_u32_e32 vcc, 22, v6
	s_nop 1
	v_cndmask_b32_e32 v27, v37, v27, vcc
	v_cmp_ne_u32_e32 vcc, 23, v6
	s_nop 1
	v_cndmask_b32_e32 v28, v37, v28, vcc
	v_cmp_ne_u32_e32 vcc, 24, v6
	s_nop 1
	v_cndmask_b32_e32 v29, v37, v29, vcc
	v_cmp_ne_u32_e32 vcc, 25, v6
	s_nop 1
	v_cndmask_b32_e32 v30, v37, v30, vcc
	v_cmp_ne_u32_e32 vcc, 26, v6
	s_nop 1
	v_cndmask_b32_e32 v31, v37, v31, vcc
	v_cmp_ne_u32_e32 vcc, 27, v6
	s_nop 1
	v_cndmask_b32_e32 v32, v37, v32, vcc
	v_cmp_ne_u32_e32 vcc, 28, v6
	s_nop 1
	v_cndmask_b32_e32 v33, v37, v33, vcc
	v_cmp_ne_u32_e32 vcc, 29, v6
	s_nop 1
	v_cndmask_b32_e32 v34, v37, v34, vcc
	v_cmp_ne_u32_e32 vcc, 30, v6
	s_nop 1
	v_cndmask_b32_e32 v35, v37, v35, vcc
	v_cmp_ne_u32_e32 vcc, 31, v6
	s_nop 1
	v_cndmask_b32_e32 v36, v37, v36, vcc
	v_cmp_gt_f32_e32 vcc, v4, v10
	s_nop 1
	v_cndmask_b32_e32 v10, v10, v4, vcc
	v_cndmask_b32_e64 v42, 0, 1, vcc
	v_cmp_gt_f32_e32 vcc, v39, v10
	s_nop 1
	v_cndmask_b32_e32 v10, v10, v39, vcc
	v_cndmask_b32_e64 v42, v42, 2, vcc
	v_cmp_gt_f32_e32 vcc, v7, v10
	s_nop 1
	v_cndmask_b32_e32 v10, v10, v7, vcc
	v_cndmask_b32_e64 v42, v42, 3, vcc
	v_cmp_gt_f32_e32 vcc, v8, v10
	s_nop 1
	v_cndmask_b32_e32 v10, v10, v8, vcc
	v_cndmask_b32_e64 v42, v42, 4, vcc
	v_cmp_gt_f32_e32 vcc, v9, v10
	s_nop 1
	v_cndmask_b32_e32 v10, v10, v9, vcc
	v_cndmask_b32_e64 v42, v42, 5, vcc
	v_cmp_gt_f32_e32 vcc, v41, v10
	s_nop 1
	v_cndmask_b32_e32 v10, v10, v41, vcc
	v_cndmask_b32_e64 v42, v42, 6, vcc
	v_cmp_gt_f32_e32 vcc, v11, v10
	s_nop 1
	v_cndmask_b32_e32 v10, v10, v11, vcc
	v_cndmask_b32_e64 v42, v42, 7, vcc
	v_cmp_gt_f32_e32 vcc, v12, v10
	s_nop 1
	v_cndmask_b32_e32 v10, v10, v12, vcc
	v_cndmask_b32_e64 v42, v42, 8, vcc
	v_cmp_gt_f32_e32 vcc, v13, v10
	s_nop 1
	v_cndmask_b32_e32 v10, v10, v13, vcc
	v_cndmask_b32_e64 v42, v42, 9, vcc
	v_cmp_gt_f32_e32 vcc, v15, v10
	s_nop 1
	v_cndmask_b32_e32 v10, v10, v15, vcc
	v_cndmask_b32_e64 v42, v42, 10, vcc
	v_cmp_gt_f32_e32 vcc, v16, v10
	s_nop 1
	v_cndmask_b32_e32 v10, v10, v16, vcc
	v_cndmask_b32_e64 v42, v42, 11, vcc
	v_cmp_gt_f32_e32 vcc, v17, v10
	s_nop 1
	v_cndmask_b32_e32 v10, v10, v17, vcc
	v_cndmask_b32_e64 v42, v42, 12, vcc
	v_cmp_gt_f32_e32 vcc, v18, v10
	s_nop 1
	v_cndmask_b32_e32 v10, v10, v18, vcc
	v_cndmask_b32_e64 v42, v42, 13, vcc
	v_cmp_gt_f32_e32 vcc, v19, v10
	s_nop 1
	v_cndmask_b32_e32 v10, v10, v19, vcc
	v_cndmask_b32_e64 v42, v42, 14, vcc
	v_cmp_gt_f32_e32 vcc, v20, v10
	s_nop 1
	v_cndmask_b32_e32 v10, v10, v20, vcc
	v_cndmask_b32_e64 v42, v42, 15, vcc
	v_cmp_gt_f32_e32 vcc, v21, v10
	s_nop 1
	v_cndmask_b32_e32 v10, v10, v21, vcc
	v_cndmask_b32_e64 v42, v42, 16, vcc
	v_cmp_gt_f32_e32 vcc, v22, v10
	s_nop 1
	v_cndmask_b32_e32 v10, v10, v22, vcc
	v_cndmask_b32_e64 v42, v42, 17, vcc
	v_cmp_gt_f32_e32 vcc, v23, v10
	s_nop 1
	v_cndmask_b32_e32 v10, v10, v23, vcc
	v_cndmask_b32_e64 v42, v42, 18, vcc
	v_cmp_gt_f32_e32 vcc, v24, v10
	s_nop 1
	v_cndmask_b32_e32 v10, v10, v24, vcc
	v_cndmask_b32_e64 v42, v42, 19, vcc
	v_cmp_gt_f32_e32 vcc, v25, v10
	s_nop 1
	v_cndmask_b32_e32 v10, v10, v25, vcc
	v_cndmask_b32_e64 v42, v42, 20, vcc
	v_cmp_gt_f32_e32 vcc, v26, v10
	s_nop 1
	v_cndmask_b32_e32 v10, v10, v26, vcc
	v_cndmask_b32_e64 v42, v42, 21, vcc
	v_cmp_gt_f32_e32 vcc, v27, v10
	s_nop 1
	v_cndmask_b32_e32 v10, v10, v27, vcc
	v_cndmask_b32_e64 v42, v42, 22, vcc
	v_cmp_gt_f32_e32 vcc, v28, v10
	s_nop 1
	v_cndmask_b32_e32 v10, v10, v28, vcc
	v_cndmask_b32_e64 v42, v42, 23, vcc
	v_cmp_gt_f32_e32 vcc, v29, v10
	s_nop 1
	v_cndmask_b32_e32 v10, v10, v29, vcc
	v_cndmask_b32_e64 v42, v42, 24, vcc
	v_cmp_gt_f32_e32 vcc, v30, v10
	s_nop 1
	v_cndmask_b32_e32 v10, v10, v30, vcc
	v_cndmask_b32_e64 v42, v42, 25, vcc
	v_cmp_gt_f32_e32 vcc, v31, v10
	s_nop 1
	v_cndmask_b32_e32 v10, v10, v31, vcc
	v_cndmask_b32_e64 v42, v42, 26, vcc
	v_cmp_gt_f32_e32 vcc, v32, v10
	s_nop 1
	v_cndmask_b32_e32 v10, v10, v32, vcc
	v_cndmask_b32_e64 v42, v42, 27, vcc
	v_cmp_gt_f32_e32 vcc, v33, v10
	s_nop 1
	v_cndmask_b32_e32 v10, v10, v33, vcc
	v_cndmask_b32_e64 v42, v42, 28, vcc
	v_cmp_gt_f32_e32 vcc, v34, v10
	s_nop 1
	v_cndmask_b32_e32 v10, v10, v34, vcc
	v_cndmask_b32_e64 v42, v42, 29, vcc
	v_cmp_gt_f32_e32 vcc, v35, v10
	s_nop 1
	v_cndmask_b32_e32 v43, v10, v35, vcc
	v_cndmask_b32_e64 v42, v42, 30, vcc
	v_cmp_gt_f32_e32 vcc, v36, v43
	s_nop 1
	v_cndmask_b32_e64 v10, v42, 31, vcc
	v_cndmask_b32_e32 v42, v43, v36, vcc
	v_cmp_ne_u32_e32 vcc, 0, v10
	s_nop 1
	v_cndmask_b32_e32 v38, v37, v38, vcc
	v_cmp_ne_u32_e32 vcc, 1, v10
	s_nop 1
	v_cndmask_b32_e32 v4, v37, v4, vcc
	v_cmp_ne_u32_e32 vcc, 2, v10
	s_nop 1
	v_cndmask_b32_e32 v39, v37, v39, vcc
	v_cmp_ne_u32_e32 vcc, 3, v10
	s_nop 1
	v_cndmask_b32_e32 v7, v37, v7, vcc
	v_cmp_ne_u32_e32 vcc, 4, v10
	s_nop 1
	v_cndmask_b32_e32 v8, v37, v8, vcc
	v_cmp_ne_u32_e32 vcc, 5, v10
	s_nop 1
	v_cndmask_b32_e32 v9, v37, v9, vcc
	v_cmp_ne_u32_e32 vcc, 6, v10
	s_nop 1
	v_cndmask_b32_e32 v41, v37, v41, vcc
	v_cmp_ne_u32_e32 vcc, 7, v10
	s_nop 1
	v_cndmask_b32_e32 v11, v37, v11, vcc
	v_cmp_ne_u32_e32 vcc, 8, v10
	s_nop 1
	v_cndmask_b32_e32 v12, v37, v12, vcc
	v_cmp_ne_u32_e32 vcc, 9, v10
	s_nop 1
	v_cndmask_b32_e32 v13, v37, v13, vcc
	v_cmp_ne_u32_e32 vcc, 10, v10
	s_nop 1
	v_cndmask_b32_e32 v15, v37, v15, vcc
	v_cmp_ne_u32_e32 vcc, 11, v10
	s_nop 1
	v_cndmask_b32_e32 v16, v37, v16, vcc
	v_cmp_ne_u32_e32 vcc, 12, v10
	s_nop 1
	v_cndmask_b32_e32 v17, v37, v17, vcc
	v_cmp_ne_u32_e32 vcc, 13, v10
	s_nop 1
	v_cndmask_b32_e32 v18, v37, v18, vcc
	v_cmp_ne_u32_e32 vcc, 14, v10
	s_nop 1
	v_cndmask_b32_e32 v19, v37, v19, vcc
	v_cmp_ne_u32_e32 vcc, 15, v10
	s_nop 1
	v_cndmask_b32_e32 v20, v37, v20, vcc
	v_cmp_ne_u32_e32 vcc, 16, v10
	s_nop 1
	v_cndmask_b32_e32 v21, v37, v21, vcc
	v_cmp_ne_u32_e32 vcc, 17, v10
	s_nop 1
	v_cndmask_b32_e32 v22, v37, v22, vcc
	v_cmp_ne_u32_e32 vcc, 18, v10
	s_nop 1
	v_cndmask_b32_e32 v23, v37, v23, vcc
	v_cmp_ne_u32_e32 vcc, 19, v10
	s_nop 1
	v_cndmask_b32_e32 v24, v37, v24, vcc
	v_cmp_ne_u32_e32 vcc, 20, v10
	s_nop 1
	v_cndmask_b32_e32 v25, v37, v25, vcc
	v_cmp_ne_u32_e32 vcc, 21, v10
	s_nop 1
	v_cndmask_b32_e32 v26, v37, v26, vcc
	v_cmp_ne_u32_e32 vcc, 22, v10
	s_nop 1
	v_cndmask_b32_e32 v27, v37, v27, vcc
	v_cmp_ne_u32_e32 vcc, 23, v10
	s_nop 1
	v_cndmask_b32_e32 v28, v37, v28, vcc
	v_cmp_ne_u32_e32 vcc, 24, v10
	s_nop 1
	v_cndmask_b32_e32 v29, v37, v29, vcc
	v_cmp_ne_u32_e32 vcc, 25, v10
	s_nop 1
	v_cndmask_b32_e32 v30, v37, v30, vcc
	v_cmp_ne_u32_e32 vcc, 26, v10
	s_nop 1
	v_cndmask_b32_e32 v31, v37, v31, vcc
	v_cmp_ne_u32_e32 vcc, 27, v10
	s_nop 1
	v_cndmask_b32_e32 v32, v37, v32, vcc
	v_cmp_ne_u32_e32 vcc, 28, v10
	s_nop 1
	v_cndmask_b32_e32 v33, v37, v33, vcc
	v_cmp_ne_u32_e32 vcc, 29, v10
	s_nop 1
	v_cndmask_b32_e32 v34, v37, v34, vcc
	v_cmp_ne_u32_e32 vcc, 30, v10
	s_nop 1
	v_cndmask_b32_e32 v35, v37, v35, vcc
	v_cmp_ne_u32_e32 vcc, 31, v10
	s_nop 1
	v_cndmask_b32_e32 v36, v37, v36, vcc
	v_max_f32_e32 v37, 0xff800000, v38
	v_cmp_gt_f32_e32 vcc, v4, v37
	s_nop 1
	v_cndmask_b32_e32 v4, v37, v4, vcc
	v_cndmask_b32_e64 v38, 0, 1, vcc
	v_cmp_gt_f32_e32 vcc, v39, v4
	s_nop 1
	v_cndmask_b32_e32 v4, v4, v39, vcc
	v_cndmask_b32_e64 v37, v38, 2, vcc
	v_cmp_gt_f32_e32 vcc, v7, v4
	s_nop 1
	v_cndmask_b32_e32 v4, v4, v7, vcc
	v_cndmask_b32_e64 v37, v37, 3, vcc
	v_cmp_gt_f32_e32 vcc, v8, v4
	s_nop 1
	v_cndmask_b32_e32 v4, v4, v8, vcc
	v_cndmask_b32_e64 v7, v37, 4, vcc
	v_cmp_gt_f32_e32 vcc, v9, v4
	s_nop 1
	v_cndmask_b32_e32 v4, v4, v9, vcc
	v_cndmask_b32_e64 v7, v7, 5, vcc
	v_cmp_gt_f32_e32 vcc, v41, v4
	s_nop 1
	v_cndmask_b32_e32 v4, v4, v41, vcc
	v_cndmask_b32_e64 v7, v7, 6, vcc
	v_cmp_gt_f32_e32 vcc, v11, v4
	s_nop 1
	v_cndmask_b32_e32 v4, v4, v11, vcc
	v_cndmask_b32_e64 v7, v7, 7, vcc
	v_cmp_gt_f32_e32 vcc, v12, v4
	s_nop 1
	v_cndmask_b32_e32 v4, v4, v12, vcc
	v_cndmask_b32_e64 v7, v7, 8, vcc
	v_cmp_gt_f32_e32 vcc, v13, v4
	s_nop 1
	v_cndmask_b32_e32 v4, v4, v13, vcc
	v_cndmask_b32_e64 v7, v7, 9, vcc
	v_cmp_gt_f32_e32 vcc, v15, v4
	s_nop 1
	v_cndmask_b32_e32 v4, v4, v15, vcc
	v_cndmask_b32_e64 v7, v7, 10, vcc
	v_cmp_gt_f32_e32 vcc, v16, v4
	v_ashrrev_i32_e32 v15, 31, v14
	v_lshlrev_b64 v[12:13], 6, v[14:15]
	v_cndmask_b32_e32 v4, v4, v16, vcc
	v_cndmask_b32_e64 v7, v7, 11, vcc
	v_cmp_gt_f32_e32 vcc, v17, v4
	v_lshl_add_u64 v[12:13], s[6:7], 0, v[12:13]
	s_nop 0
	v_cndmask_b32_e32 v4, v4, v17, vcc
	v_cndmask_b32_e64 v7, v7, 12, vcc
	v_cmp_gt_f32_e32 vcc, v18, v4
	s_nop 1
	v_cndmask_b32_e32 v4, v4, v18, vcc
	v_cndmask_b32_e64 v7, v7, 13, vcc
	v_cmp_gt_f32_e32 vcc, v19, v4
	s_nop 1
	v_cndmask_b32_e32 v4, v4, v19, vcc
	v_cndmask_b32_e64 v7, v7, 14, vcc
	v_cmp_gt_f32_e32 vcc, v20, v4
	s_nop 1
	v_cndmask_b32_e32 v4, v4, v20, vcc
	v_cndmask_b32_e64 v7, v7, 15, vcc
	v_cmp_gt_f32_e32 vcc, v21, v4
	s_nop 1
	v_cndmask_b32_e32 v11, v4, v21, vcc
	v_lshlrev_b32_e32 v4, 5, v2
	v_lshl_add_u64 v[8:9], v[4:5], 2, s[10:11]
	global_atomic_add v8, v[8:9], v1, off sc0
	v_cndmask_b32_e64 v7, v7, 16, vcc
	v_cmp_gt_f32_e32 vcc, v22, v11
	v_sub_f32_e32 v9, v40, v3
	v_mul_f32_e32 v9, 0x3fb8aa3b, v9
	v_cndmask_b32_e64 v4, v7, 17, vcc
	v_cndmask_b32_e32 v7, v11, v22, vcc
	v_cmp_gt_f32_e32 vcc, v23, v7
	v_exp_f32_e32 v11, v9
	v_sub_f32_e32 v9, v42, v3
	v_cndmask_b32_e32 v7, v7, v23, vcc
	v_cndmask_b32_e64 v4, v4, 18, vcc
	v_cmp_gt_f32_e32 vcc, v24, v7
	v_mul_f32_e32 v9, 0x3fb8aa3b, v9
	v_exp_f32_e32 v17, v9
	v_cndmask_b32_e32 v7, v7, v24, vcc
	v_cndmask_b32_e64 v4, v4, 19, vcc
	v_cmp_gt_f32_e32 vcc, v25, v7
	s_nop 1
	v_cndmask_b32_e32 v7, v7, v25, vcc
	v_cndmask_b32_e64 v4, v4, 20, vcc
	v_cmp_gt_f32_e32 vcc, v26, v7
	s_nop 1
	v_cndmask_b32_e32 v7, v7, v26, vcc
	v_cndmask_b32_e64 v4, v4, 21, vcc
	v_cmp_gt_f32_e32 vcc, v27, v7
	s_nop 1
	v_cndmask_b32_e32 v7, v7, v27, vcc
	v_cndmask_b32_e64 v4, v4, 22, vcc
	v_cmp_gt_f32_e32 vcc, v28, v7
	s_nop 1
	v_cndmask_b32_e32 v7, v7, v28, vcc
	v_cndmask_b32_e64 v4, v4, 23, vcc
	v_cmp_gt_f32_e32 vcc, v29, v7
	s_nop 1
	v_cndmask_b32_e32 v7, v7, v29, vcc
	v_cndmask_b32_e64 v4, v4, 24, vcc
	v_cmp_gt_f32_e32 vcc, v30, v7
	s_nop 1
	v_cndmask_b32_e32 v7, v7, v30, vcc
	v_cndmask_b32_e64 v4, v4, 25, vcc
	v_cmp_gt_f32_e32 vcc, v31, v7
	s_nop 1
	v_cndmask_b32_e32 v7, v7, v31, vcc
	v_cndmask_b32_e64 v4, v4, 26, vcc
	v_cmp_gt_f32_e32 vcc, v32, v7
	s_nop 1
	v_cndmask_b32_e32 v7, v7, v32, vcc
	v_cndmask_b32_e64 v4, v4, 27, vcc
	v_cmp_gt_f32_e32 vcc, v33, v7
	s_nop 1
	v_cndmask_b32_e32 v7, v7, v33, vcc
	v_cndmask_b32_e64 v4, v4, 28, vcc
	v_cmp_gt_f32_e32 vcc, v34, v7
	s_nop 1
	v_cndmask_b32_e32 v7, v7, v34, vcc
	v_cndmask_b32_e64 v4, v4, 29, vcc
	v_cmp_gt_f32_e32 vcc, v35, v7
	s_nop 1
	v_cndmask_b32_e32 v7, v7, v35, vcc
	v_cndmask_b32_e64 v4, v4, 30, vcc
	v_cmp_gt_f32_e32 vcc, v36, v7
	s_nop 1
	v_cndmask_b32_e64 v16, v4, 31, vcc
	v_lshlrev_b32_e32 v70, 5, v6
	v_mov_b32_e32 v71, v5
	v_lshl_add_u64 v[70:71], v[70:71], 2, s[10:11]
	global_atomic_add v74, v[70:71], v1, off sc0
	v_lshlrev_b32_e32 v70, 5, v10
	v_mov_b32_e32 v71, v5
	v_lshl_add_u64 v[70:71], v[70:71], 2, s[10:11]
	global_atomic_add v75, v[70:71], v1, off sc0
	v_lshlrev_b32_e32 v70, 5, v16
	v_mov_b32_e32 v71, v5
	v_lshl_add_u64 v[70:71], v[70:71], 2, s[10:11]
	global_atomic_add v76, v[70:71], v1, off sc0
	v_cndmask_b32_e32 v4, v7, v36, vcc
	v_sub_f32_e32 v7, v3, v3
	v_mul_f32_e32 v7, 0x3fb8aa3b, v7
	v_exp_f32_e32 v7, v7
	v_sub_f32_e32 v3, v4, v3
	v_mul_f32_e32 v3, 0x3fb8aa3b, v3
	v_exp_f32_e32 v22, v3
	v_add_f32_e32 v3, 0, v7
	v_add_f32_e32 v3, v3, v11
	v_add_f32_e32 v3, v3, v17
	v_add_f32_e32 v3, v3, v22
	v_div_scale_f32 v4, s[2:3], v3, v3, 1.0
	v_rcp_f32_e32 v9, v4
	s_mov_b32 s2, 0x5e30000
	v_fma_f32 v15, -v4, v9, 1.0
	v_fmac_f32_e32 v9, v15, v9
	v_div_scale_f32 v15, vcc, 1.0, v3, 1.0
	v_mul_f32_e32 v18, v15, v9
	v_fma_f32 v19, -v4, v18, v15
	v_fmac_f32_e32 v18, v19, v9
	v_fma_f32 v4, -v4, v18, v15
	v_div_fmas_f32 v4, v4, v9, v18
	v_div_fixup_f32 v15, v4, v3, 1.0
	v_mov_b32_e32 v3, v5
	v_lshlrev_b64 v[18:19], 16, v[2:3]
	s_waitcnt vmcnt(0)
	v_ashrrev_i32_e32 v9, 31, v8
	v_lshl_add_u64 v[18:19], s[8:9], 0, v[18:19]
	v_lshl_add_u64 v[18:19], v[8:9], 2, v[18:19]
	v_mov_b32_e32 v3, v8
	v_add_co_u32_e32 v8, vcc, s2, v12
	v_mul_f32_e32 v4, v7, v15
	s_nop 0
	v_addc_co_u32_e32 v9, vcc, 0, v13, vcc
	global_store_dword v[18:19], v14, off
	global_store_dwordx4 v[8:9], v[2:5], off
	v_mov_b32_e32 v7, v5
	v_lshlrev_b64 v[8:9], 16, v[6:7]
	v_mov_b32_e32 v2, v74
	v_lshl_add_u64 v[8:9], s[8:9], 0, v[8:9]
	s_mov_b64 s[2:3], 0x5e30000
	v_lshl_add_u64 v[20:21], v[12:13], 0, s[2:3]
	v_lshlrev_b32_e32 v4, 5, v10
	v_mul_f32_e32 v12, v17, v15
	v_mov_b32_e32 v13, v5
	v_mov_b32_e32 v17, v5
	v_mul_f32_e32 v18, v22, v15
	v_mov_b32_e32 v19, v5
	v_ashrrev_i32_e32 v3, 31, v2
	v_lshl_add_u64 v[8:9], v[2:3], 2, v[8:9]
	global_store_dword v[8:9], v14, off
	v_mul_f32_e32 v8, v11, v15
	v_mov_b32_e32 v7, v2
	v_mov_b32_e32 v9, v5
	global_store_dwordx4 v[20:21], v[6:9], off offset:16
	v_mov_b32_e32 v2, v75
	v_mov_b32_e32 v11, v5
	v_lshlrev_b64 v[6:7], 16, v[10:11]
	v_lshl_add_u64 v[6:7], s[8:9], 0, v[6:7]
	v_lshlrev_b32_e32 v4, 5, v16
	v_ashrrev_i32_e32 v3, 31, v2
	v_lshl_add_u64 v[6:7], v[2:3], 2, v[6:7]
	v_mov_b32_e32 v11, v2
	global_store_dword v[6:7], v14, off
	global_store_dwordx4 v[20:21], v[10:13], off offset:32
	v_mov_b32_e32 v2, v76
	v_lshlrev_b64 v[6:7], 16, v[16:17]
	v_lshl_add_u64 v[6:7], s[8:9], 0, v[6:7]
	v_ashrrev_i32_e32 v3, 31, v2
	v_lshl_add_u64 v[6:7], v[2:3], 2, v[6:7]
	v_mov_b32_e32 v17, v2
	global_store_dword v[6:7], v14, off
	global_store_dwordx4 v[20:21], v[16:19], off offset:48
